# NA job prologue now requests all 8-9 initial key-ring rows before waiting (was load-wait-write per row)
# baseline (speedup 1.0000x reference)
; #define LAS __attribute__((address_space(3)))
; __device__ __forceinline__ void ph_na(Frame& F, int l, bool last) {
;     ...
;           const int lo = na_kr0(half * 32), hi0 = na_kr0(half * 32 + 1) + 7;
;           for (int kr = lo; kr <= hi0; ++kr) *(LAS bf16x8*)(kdst + (kr % 9) * 64 * 72) = gld16(krow + (size_t)kr * 64 * DIN); }
;         __syncthreads();
.LBB0_480:
	s_mov_b64 s[20:21], 0x68000
	global_load_dwordx4 v[6:9], v[2:3], off
	s_add_i32 s0, s19, 1
	s_cmp_gt_u32 s0, s73
	s_cbranch_scc1 .Lrf_issued
	v_lshl_add_u64 v[2:3], v[2:3], 0, s[20:21]
	global_load_dwordx4 v[10:13], v[2:3], off
	s_add_i32 s0, s19, 2
	s_cmp_gt_u32 s0, s73
	s_cbranch_scc1 .Lrf_issued
	v_lshl_add_u64 v[2:3], v[2:3], 0, s[20:21]
	global_load_dwordx4 v[14:17], v[2:3], off
	s_add_i32 s0, s19, 3
	s_cmp_gt_u32 s0, s73
	s_cbranch_scc1 .Lrf_issued
	v_lshl_add_u64 v[2:3], v[2:3], 0, s[20:21]
	global_load_dwordx4 v[18:21], v[2:3], off
	s_add_i32 s0, s19, 4
	s_cmp_gt_u32 s0, s73
	s_cbranch_scc1 .Lrf_issued
	v_lshl_add_u64 v[2:3], v[2:3], 0, s[20:21]
	global_load_dwordx4 v[22:25], v[2:3], off
	s_add_i32 s0, s19, 5
	s_cmp_gt_u32 s0, s73
	s_cbranch_scc1 .Lrf_issued
	v_lshl_add_u64 v[2:3], v[2:3], 0, s[20:21]
	global_load_dwordx4 v[26:29], v[2:3], off
	s_add_i32 s0, s19, 6
	s_cmp_gt_u32 s0, s73
	s_cbranch_scc1 .Lrf_issued
	v_lshl_add_u64 v[2:3], v[2:3], 0, s[20:21]
	global_load_dwordx4 v[30:33], v[2:3], off
	s_add_i32 s0, s19, 7
	s_cmp_gt_u32 s0, s73
	s_cbranch_scc1 .Lrf_issued
	v_lshl_add_u64 v[2:3], v[2:3], 0, s[20:21]
	global_load_dwordx4 v[34:37], v[2:3], off
	s_add_i32 s0, s19, 8
	s_cmp_gt_u32 s0, s73
	s_cbranch_scc1 .Lrf_issued
	v_lshl_add_u64 v[2:3], v[2:3], 0, s[20:21]
	global_load_dwordx4 v[38:41], v[2:3], off
.Lrf_issued:
	s_waitcnt vmcnt(0)
	s_mov_b32 s21, s19
	s_mul_i32 s0, s21, 57
	s_bfe_u32 s0, s0, 0x70009
	s_mul_i32 s0, s0, 9
	s_sub_i32 s0, s21, s0
	s_and_b32 s0, s0, 0xff
	s_mulk_i32 s0, 0x2400
	v_add_u32_e32 v5, s0, v97
	ds_write_b128 v5, v[6:9]
	s_add_i32 s21, s19, 1
	s_cmp_gt_u32 s21, s73
	s_cbranch_scc1 .Lrf_done
	s_mul_i32 s0, s21, 57
	s_bfe_u32 s0, s0, 0x70009
	s_mul_i32 s0, s0, 9
	s_sub_i32 s0, s21, s0
	s_and_b32 s0, s0, 0xff
	s_mulk_i32 s0, 0x2400
	v_add_u32_e32 v5, s0, v97
	ds_write_b128 v5, v[10:13]
	s_add_i32 s21, s19, 2
	s_cmp_gt_u32 s21, s73
	s_cbranch_scc1 .Lrf_done
	s_mul_i32 s0, s21, 57
	s_bfe_u32 s0, s0, 0x70009
	s_mul_i32 s0, s0, 9
	s_sub_i32 s0, s21, s0
	s_and_b32 s0, s0, 0xff
	s_mulk_i32 s0, 0x2400
	v_add_u32_e32 v5, s0, v97
	ds_write_b128 v5, v[14:17]
	s_add_i32 s21, s19, 3
	s_cmp_gt_u32 s21, s73
	s_cbranch_scc1 .Lrf_done
	s_mul_i32 s0, s21, 57
	s_bfe_u32 s0, s0, 0x70009
	s_mul_i32 s0, s0, 9
	s_sub_i32 s0, s21, s0
	s_and_b32 s0, s0, 0xff
	s_mulk_i32 s0, 0x2400
	v_add_u32_e32 v5, s0, v97
	ds_write_b128 v5, v[18:21]
	s_add_i32 s21, s19, 4
	s_cmp_gt_u32 s21, s73
	s_cbranch_scc1 .Lrf_done
	s_mul_i32 s0, s21, 57
	s_bfe_u32 s0, s0, 0x70009
	s_mul_i32 s0, s0, 9
	s_sub_i32 s0, s21, s0
	s_and_b32 s0, s0, 0xff
	s_mulk_i32 s0, 0x2400
	v_add_u32_e32 v5, s0, v97
	ds_write_b128 v5, v[22:25]
	s_add_i32 s21, s19, 5
	s_cmp_gt_u32 s21, s73
	s_cbranch_scc1 .Lrf_done
	s_mul_i32 s0, s21, 57
	s_bfe_u32 s0, s0, 0x70009
	s_mul_i32 s0, s0, 9
	s_sub_i32 s0, s21, s0
	s_and_b32 s0, s0, 0xff
	s_mulk_i32 s0, 0x2400
	v_add_u32_e32 v5, s0, v97
	ds_write_b128 v5, v[26:29]
	s_add_i32 s21, s19, 6
	s_cmp_gt_u32 s21, s73
	s_cbranch_scc1 .Lrf_done
	s_mul_i32 s0, s21, 57
	s_bfe_u32 s0, s0, 0x70009
	s_mul_i32 s0, s0, 9
	s_sub_i32 s0, s21, s0
	s_and_b32 s0, s0, 0xff
	s_mulk_i32 s0, 0x2400
	v_add_u32_e32 v5, s0, v97
	ds_write_b128 v5, v[30:33]
	s_add_i32 s21, s19, 7
	s_cmp_gt_u32 s21, s73
	s_cbranch_scc1 .Lrf_done
	s_mul_i32 s0, s21, 57
	s_bfe_u32 s0, s0, 0x70009
	s_mul_i32 s0, s0, 9
	s_sub_i32 s0, s21, s0
	s_and_b32 s0, s0, 0xff
	s_mulk_i32 s0, 0x2400
	v_add_u32_e32 v5, s0, v97
	ds_write_b128 v5, v[34:37]
	s_add_i32 s21, s19, 8
	s_cmp_gt_u32 s21, s73
	s_cbranch_scc1 .Lrf_done
	s_mul_i32 s0, s21, 57
	s_bfe_u32 s0, s0, 0x70009
	s_mul_i32 s0, s0, 9
	s_sub_i32 s0, s21, s0
	s_and_b32 s0, s0, 0xff
	s_mulk_i32 s0, 0x2400
	v_add_u32_e32 v5, s0, v97
	ds_write_b128 v5, v[38:41]
.Lrf_done:
	s_lshl_b32 s0, s4, 11
	s_mulk_i32 s3, 0x2200
	s_mul_hi_u32 s4, s2, 0x2200
	s_sub_i32 s75, 0, s70
	s_add_i32 s76, s58, s70
	s_lshl_b32 s22, s5, 1
	s_add_i32 s4, s4, s3
	s_add_u32 s77, s42, s22
	s_mulk_i32 s2, 0x2200
	s_addc_u32 s78, s43, 0
	s_add_u32 s79, s62, s2
	s_addc_u32 s80, s63, s4
	v_lshl_add_u64 v[0:1], s[42:43], 0, v[0:1]
	s_add_u32 s81, s64, s22
	v_lshl_add_u64 v[0:1], v[0:1], 0, s[22:23]
	v_lshlrev_b32_e32 v192, 1, v4
	s_addc_u32 s82, s65, 0
	s_add_i32 s2, s67, s18
	s_mov_b32 s74, 0
	v_lshl_add_u64 v[88:89], v[0:1], 0, v[192:193]
	s_add_i32 s48, s2, s0
	s_waitcnt lgkmcnt(0)
	s_barrier
	s_branch .LBB0_483
